# one static priority raise for the wave half 4..7 in the attention phase (the compiled s_setprio 2 was unconditional: all eight waves ran at the same priority)
# baseline (speedup 1.0000x reference)
; #define LAS __attribute__((address_space(3)))
; __global__ void __launch_bounds__(NTHREADS, 2) fwd_kernel(Args args) {
;     ...
;         for (int i = tid; i < 16 * 132; i += NTHREADS) lut[i] = ((const float*)(ws + WS_TAB + TAB_LUT))[i];
;         __syncthreads();
;         if ((tid >> 6) >= 4) __builtin_amdgcn_s_setprio(2);
;         for (int i = 0; i < 16; ++i) { const int bg = 8 * (i >> 2) + ((int)blockIdx.x & 7), wi = (int)blockIdx.x >> 3, k = i & 3;
;             const int tau = k == 0 ? wi : k == 1 ? 63 - wi : k == 2 ? 64 + wi : 127 - wi;
;             if (k == 0) {
;                 __syncthreads();
;                 LAS float* nbt = (LAS float*)(lds + NB_OFF);
;                 for (int x = tid; x < 16 * 264; x += NTHREADS) { const int rr = x / 1056, sh = (x / 264) & 3, z = x % 264, d = 196 - z - sh;
;                     nbt[x] = d < 0 ? -__builtin_inff() : lut[((bg & 3) * 4 + rr) * 132 + (d > 128 ? 128 : d)]; }
;                 __syncthreads();
;             }
;             nsa_unit(ws, lds, lut, bg >> 2, bg & 3, tau, tid); }
;         __builtin_amdgcn_s_setprio(0);
.LBB0_1015:
	global_load_dword v6, v[2:3], off
	v_add_u32_e32 v4, 0x200, v4
	v_cmp_lt_u32_e32 vcc, s0, v4
	v_lshl_add_u64 v[2:3], v[2:3], 0, s[10:11]
	s_or_b64 s[8:9], vcc, s[8:9]
	s_waitcnt vmcnt(0)
	ds_write_b32 v5, v6
	v_add_u32_e32 v5, 0x800, v5
	s_andn2_b64 exec, exec, s[8:9]
	s_cbranch_execnz .LBB0_1015
	v_writelane_b32 v253, s2, 20
	s_nop 1
	v_writelane_b32 v253, s3, 21
	s_or_b64 exec, exec, s[8:9]
	s_movk_i32 s0, 0xff
	v_cmp_lt_u32_e32 vcc, s0, v0
	s_waitcnt lgkmcnt(0)
	s_barrier
	s_and_saveexec_b64 s[8:9], vcc
	s_setprio 2
	s_or_b64 exec, exec, s[8:9]
	v_readfirstlane_b32 s2, v0
	s_cmp_gt_u32 s2, 0xff
	s_cbranch_scc1 .Lp5_hi
	s_setprio 0
.Lp5_hi:
	v_readlane_b32 s2, v253, 11
	s_ashr_i32 s82, s2, 3
	s_add_i32 s0, s82, 64
	v_writelane_b32 v253, s0, 22
	s_sub_i32 s0, 0x7f, s82
	v_writelane_b32 v253, s0, 26
	s_sub_i32 s0, 63, s82
	s_and_b32 s52, s2, 3
	v_writelane_b32 v253, s0, 28
	s_lshl_b32 s0, s2, 2
	s_and_b32 s35, s2, 4
	s_and_b32 s74, s0, 12
	s_lshl_b32 s89, s52, 2
	s_add_u32 s87, s6, 0xd800000
	s_addc_u32 s90, s7, 0
	s_lshl_b32 s78, s52, 7
	s_add_u32 s0, s6, 0x37600000
	v_writelane_b32 v253, s0, 29
	s_addc_u32 s0, s7, 0
	v_writelane_b32 v253, s0, 30
	s_add_u32 s0, s6, s78
	s_addc_u32 s1, s7, 0
	s_add_u32 s3, s0, 0x37400000
	v_writelane_b32 v253, s3, 31
	s_addc_u32 s3, s1, 0
	v_writelane_b32 v253, s3, 32
	s_add_u32 s3, s6, 0x19800000
	v_writelane_b32 v253, s3, 34
	s_addc_u32 s3, s7, 0
	v_writelane_b32 v253, s3, 35
	s_add_u32 s3, s6, 0x1b800000
	v_writelane_b32 v253, s3, 36
	s_addc_u32 s3, s7, 0
	s_add_u32 s28, s6, 0x31800000
	s_addc_u32 s29, s7, 0
	v_writelane_b32 v253, s3, 37
	s_add_u32 s3, s6, 0x1d800000
	v_writelane_b32 v253, s3, 38
	s_addc_u32 s3, s7, 0
	v_writelane_b32 v253, s3, 39
	s_add_u32 s3, s6, 0x1f800000
	v_writelane_b32 v253, s3, 40
	s_addc_u32 s3, s7, 0
	s_add_u32 s30, s6, 0x31800004
	s_addc_u32 s31, s7, 0
	s_add_u32 s40, s6, 0x31800008
	s_addc_u32 s41, s7, 0
	s_add_u32 s42, s6, 0x1800000
	s_addc_u32 s43, s7, 0
	v_writelane_b32 v253, s3, 41
	s_add_u32 s3, s0, 0x37408000
	v_writelane_b32 v253, s3, 42
	s_addc_u32 s3, s1, 0
	s_lshl_b32 s2, s2, 16
	v_writelane_b32 v253, s3, 44
	s_and_b32 s2, s2, 0x40000
	v_writelane_b32 v253, s2, 46
	s_add_u32 s2, s6, 0x37600080
	s_addc_u32 s3, s7, 0
	s_or_b32 s94, s35, s52
	s_add_u32 s95, s0, 0x19810000
	s_addc_u32 s96, s1, 0
	s_add_u32 s97, s6, 0x1b800100
	v_writelane_b32 v253, s2, 47
	s_addc_u32 s4, s7, 0
	s_add_u32 s0, s0, 0x1d7c8000
	v_writelane_b32 v253, s3, 48
	v_writelane_b32 v253, s0, 49
	s_addc_u32 s0, s1, 0
	v_writelane_b32 v253, s0, 50
	s_add_u32 s0, s6, 0x1f7ffc80
	v_writelane_b32 v253, s0, 51
	s_addc_u32 s0, s7, 0
	v_add_u32_e32 v151, 0x23d40, v1
	v_writelane_b32 v253, s0, 53
	s_add_i32 s25, 0, 0x20c00
	v_mbcnt_lo_u32_b32 v1, -1, 0
	s_add_i32 s1, 0, 0x24040
	s_mov_b32 s27, 0
	s_movk_i32 s56, 0x200
	v_mov_b32_e32 v153, 0
	s_add_i32 s57, 0, 0x20850
	s_add_i32 s34, 0, 0x20854
	s_mov_b64 s[46:47], 0x8000
	s_mov_b64 s[48:49], 0x80
	v_mbcnt_hi_u32_b32 v176, -1, v1
	s_movk_i32 s0, 0xc0
	v_writelane_b32 v253, s1, 54
	s_mov_b32 s20, 0x3f803f80
	s_mov_b32 s54, 0x7cf0bdc2
	v_mov_b32_e32 v177, 1
	s_add_i32 s1, 0, 0x23840
	v_mov_b32_e32 v178, 3
	v_mov_b32_e32 v179, s25
	v_mov_b32_e32 v180, 0x80
	v_mov_b32_e32 v2, 0xff800000
	v_mov_b32_e32 v181, 0x100000
	v_mov_b32_e32 v182, 0x41
	s_mov_b32 s80, 0
	s_mov_b32 s81, 0
	v_writelane_b32 v253, s1, 56
	s_branch .LBB0_1021
